# P11/P14 (rotated K-loops) first iteration peeled with C=0 as well; P23 header drops zeroing of registers the rewritten epilogue no longer uses
# speedup vs baseline: 1.0037x; 1.0037x over previous
.LBB0_1395:
	s_and_b32 s89, s84, 1
	s_andn2_b64 vcc, exec, s[18:19]
	s_cbranch_vccnz .Lzs_5
	s_min_i32 s30, s86, 0x80
	s_mul_hi_i32 s94, s85, 0x2e8ba2e9
	s_lshr_b32 s30, s30, 5
	s_lshr_b32 s95, s94, 31
	s_lshr_b32 s94, s94, 3
	s_mulk_i32 s30, 0x2c00
	s_add_i32 s94, s94, s95
	s_ashr_i32 s31, s30, 31
	s_mul_i32 s94, s94, 44
	s_lshl_b32 s75, s89, 10
	s_or_b64 s[4:5], s[4:5], s[6:7]
	s_sub_i32 s94, s85, s94
	s_lshl_b64 s[30:31], s[30:31], 2
	s_add_u32 s95, s25, s30
	s_addc_u32 s96, s35, s31
	s_lshl_b32 s30, s94, 7
	s_ashr_i32 s31, s30, 31
	s_lshl_b64 s[30:31], s[30:31], 2
	s_add_u32 s30, s95, s30
	s_addc_u32 s31, s96, s31
	v_mov_b32_e32 v169, v163
	v_lshl_add_u64 v[2:3], s[30:31], 0, v[168:169]
	v_mov_b32_e32 v171, v163
	s_add_i32 s95, s75, 0
	v_lshl_add_u64 v[172:173], v[2:3], 0, v[170:171]
	s_addk_i32 s92, 0x80
	s_addk_i32 s93, 0x100
	s_mov_b32 s94, 0
	s_add_i32 s95, s95, 0x21400
	s_cmp_lg_u32 s67, s94
	s_cselect_b64 s[30:31], -1, 0
	s_or_b64 s[96:97], s[30:31], s[4:5]
	s_and_b64 vcc, exec, s[96:97]
	s_cbranch_vccnz .Lphr_0
	s_mov_b32 m0, s95
	s_nop 0
	global_load_lds_dwordx4 v[172:173], off
.Lphr_0:
	ds_read_b128 v[18:21], v177
	ds_read_b128 v[22:25], v178
	ds_read_b128 v[26:29], v185
	ds_read_b128 v[30:33], v186
	ds_read_b128 v[2:5], v179
	ds_read_b128 v[6:9], v180
	ds_read_b128 v[10:13], v187
	ds_read_b128 v[14:17], v188
	s_add_i32 s75, s92, 0x80
	s_and_b64 s[30:31], s[30:31], exec
	s_cselect_b32 s75, s75, s91
	s_cselect_b32 s96, s93, s29
	s_add_i32 s30, s75, 0x80
	s_add_i32 s31, s96, 0x80
	v_mov_b32_e32 v162, v1
	ds_read_b128 v[198:201], v193
	ds_read_b128 v[202:205], v193 offset:1024
	ds_read_b128 v[214:217], v193 offset:2048
	ds_read_b128 v[218:221], v193 offset:3072
	ds_read_b128 v[222:225], v193 offset:4096
	ds_read_b128 v[226:229], v193 offset:5120
	ds_read_b128 v[230:233], v193 offset:6144
	ds_read_b128 v[234:237], v193 offset:7168
	s_add_i32 s97, s92, s65
	v_add_u32_e32 v162, s97, v162
	s_add_i32 m0, s47, 0xc000
	s_add_i32 s97, s92, s74
	global_load_lds_dwordx4 v162, s[10:11]
	v_mov_b32_e32 v162, v1
	s_add_i32 m0, s47, 0xe000
	v_add_u32_e32 v162, s97, v162
	global_load_lds_dwordx4 v162, s[10:11]
	s_waitcnt vmcnt(8)
	s_waitcnt lgkmcnt(0)
	s_barrier
	s_setprio 1
	s_waitcnt lgkmcnt(0)
	v_mfma_f32_16x16x128_f8f6f4 v[158:161], v[18:25], v[198:205], 0
	v_mfma_f32_16x16x128_f8f6f4 v[150:153], v[26:33], v[198:205], 0
	v_mfma_f32_16x16x128_f8f6f4 v[142:145], v[18:25], v[214:221], 0
	v_mfma_f32_16x16x128_f8f6f4 v[134:137], v[26:33], v[214:221], 0
	v_mfma_f32_16x16x128_f8f6f4 v[126:129], v[18:25], v[222:229], 0
	v_mfma_f32_16x16x128_f8f6f4 v[118:121], v[26:33], v[222:229], 0
	v_mfma_f32_16x16x128_f8f6f4 v[110:113], v[18:25], v[230:237], 0
	v_mfma_f32_16x16x128_f8f6f4 v[102:105], v[26:33], v[230:237], 0
	s_setprio 0
	s_setprio 1
	v_mfma_f32_16x16x128_f8f6f4 v[154:157], v[2:9], v[198:205], 0
	v_mfma_f32_16x16x128_f8f6f4 v[146:149], v[10:17], v[198:205], 0
	v_mfma_f32_16x16x128_f8f6f4 v[138:141], v[2:9], v[214:221], 0
	v_mfma_f32_16x16x128_f8f6f4 v[130:133], v[10:17], v[214:221], 0
	v_mfma_f32_16x16x128_f8f6f4 v[122:125], v[2:9], v[222:229], 0
	v_mfma_f32_16x16x128_f8f6f4 v[114:117], v[10:17], v[222:229], 0
	v_mfma_f32_16x16x128_f8f6f4 v[106:109], v[2:9], v[230:237], 0
	v_mfma_f32_16x16x128_f8f6f4 v[98:101], v[10:17], v[230:237], 0
	s_setprio 0
	s_barrier
	v_mov_b32_e32 v162, v174
	ds_read_b128 v[198:201], v193 offset:16384
	ds_read_b128 v[202:205], v193 offset:17408
	ds_read_b128 v[214:217], v193 offset:18432
	ds_read_b128 v[218:221], v193 offset:19456
	ds_read_b128 v[222:225], v193 offset:20480
	ds_read_b128 v[226:229], v193 offset:21504
	ds_read_b128 v[230:233], v193 offset:22528
	ds_read_b128 v[234:237], v193 offset:23552
	s_mov_b32 m0, s48
	v_add_u32_e32 v162, s96, v162
	global_load_lds_dwordx4 v162, s[20:21]
	v_mov_b32_e32 v162, v174
	s_add_i32 s96, s96, s46
	v_add_u32_e32 v162, s96, v162
	s_mov_b32 m0, s49
	s_add_i32 s96, s96, s46
	global_load_lds_dwordx4 v162, s[20:21]
	v_mov_b32_e32 v162, v174
	s_mov_b32 m0, s50
	v_add_u32_e32 v162, s96, v162
	global_load_lds_dwordx4 v162, s[20:21]
	v_mov_b32_e32 v162, v174
	s_add_i32 s96, s96, s46
	v_add_u32_e32 v162, s96, v162
	s_mov_b32 m0, s51
	s_nop 0
	global_load_lds_dwordx4 v162, s[20:21]
	v_mov_b32_e32 v162, v1
	s_mov_b32 m0, s47
	v_add_u32_e32 v162, s75, v162
	global_load_lds_dwordx4 v162, s[10:11]
	v_mov_b32_e32 v162, v1
	s_add_i32 s75, s75, s45
	v_add_u32_e32 v162, s75, v162
	s_mov_b32 m0, s52
	s_nop 0
	global_load_lds_dwordx4 v162, s[10:11]
	s_waitcnt vmcnt(8)
	s_waitcnt lgkmcnt(0)
	s_barrier
	s_setprio 1
	s_waitcnt lgkmcnt(0)
	v_mfma_f32_16x16x128_f8f6f4 v[94:97], v[18:25], v[198:205], 0
	v_mfma_f32_16x16x128_f8f6f4 v[86:89], v[26:33], v[198:205], 0
	v_mfma_f32_16x16x128_f8f6f4 v[78:81], v[18:25], v[214:221], 0
	v_mfma_f32_16x16x128_f8f6f4 v[70:73], v[26:33], v[214:221], 0
	v_mfma_f32_16x16x128_f8f6f4 v[62:65], v[18:25], v[222:229], 0
	v_mfma_f32_16x16x128_f8f6f4 v[54:57], v[26:33], v[222:229], 0
	v_mfma_f32_16x16x128_f8f6f4 v[46:49], v[18:25], v[230:237], 0
	v_mfma_f32_16x16x128_f8f6f4 v[38:41], v[26:33], v[230:237], 0
	s_setprio 0
	s_setprio 1
	v_mfma_f32_16x16x128_f8f6f4 v[90:93], v[2:9], v[198:205], 0
	v_mfma_f32_16x16x128_f8f6f4 v[82:85], v[10:17], v[198:205], 0
	v_mfma_f32_16x16x128_f8f6f4 v[74:77], v[2:9], v[214:221], 0
	v_mfma_f32_16x16x128_f8f6f4 v[66:69], v[10:17], v[214:221], 0
	v_mfma_f32_16x16x128_f8f6f4 v[58:61], v[2:9], v[222:229], 0
	v_mfma_f32_16x16x128_f8f6f4 v[50:53], v[10:17], v[222:229], 0
	v_mfma_f32_16x16x128_f8f6f4 v[42:45], v[2:9], v[230:237], 0
	v_mfma_f32_16x16x128_f8f6f4 v[34:37], v[10:17], v[230:237], 0
	s_setprio 0
	s_barrier
	s_branch .Lmidr_0

.Lmidr_0:
	ds_read_b128 v[2:5], v181
	ds_read_b128 v[6:9], v182
	ds_read_b128 v[10:13], v189
	ds_read_b128 v[14:17], v190
	ds_read_b128 v[18:21], v183
	ds_read_b128 v[22:25], v184
	ds_read_b128 v[26:29], v191
	ds_read_b128 v[30:33], v192
	v_mov_b32_e32 v162, v1
	ds_read_b128 v[198:201], v193 offset:32768
	ds_read_b128 v[202:205], v193 offset:33792
	ds_read_b128 v[214:217], v193 offset:34816
	ds_read_b128 v[218:221], v193 offset:35840
	ds_read_b128 v[222:225], v193 offset:36864
	ds_read_b128 v[226:229], v193 offset:37888
	ds_read_b128 v[230:233], v193 offset:38912
	ds_read_b128 v[234:237], v193 offset:39936
	s_add_i32 s75, s75, s45
	s_mov_b32 m0, s53
	v_add_u32_e32 v162, s75, v162
	global_load_lds_dwordx4 v162, s[10:11]
	v_mov_b32_e32 v162, v1
	s_add_i32 s75, s75, s45
	v_add_u32_e32 v162, s75, v162
	s_mov_b32 m0, s54
	s_nop 0
	global_load_lds_dwordx4 v162, s[10:11]
	s_waitcnt vmcnt(8)
	s_waitcnt lgkmcnt(0)
	s_barrier
	s_setprio 1
	s_waitcnt lgkmcnt(0)
	v_mfma_f32_16x16x128_f8f6f4 v[158:161], v[2:9], v[198:205], v[158:161]
	v_mfma_f32_16x16x128_f8f6f4 v[150:153], v[10:17], v[198:205], v[150:153]
	v_mfma_f32_16x16x128_f8f6f4 v[142:145], v[2:9], v[214:221], v[142:145]
	v_mfma_f32_16x16x128_f8f6f4 v[134:137], v[10:17], v[214:221], v[134:137]
	v_mfma_f32_16x16x128_f8f6f4 v[126:129], v[2:9], v[222:229], v[126:129]
	v_mfma_f32_16x16x128_f8f6f4 v[118:121], v[10:17], v[222:229], v[118:121]
	v_mfma_f32_16x16x128_f8f6f4 v[110:113], v[2:9], v[230:237], v[110:113]
	v_mfma_f32_16x16x128_f8f6f4 v[102:105], v[10:17], v[230:237], v[102:105]
	s_setprio 0
	s_setprio 1
	v_mfma_f32_16x16x128_f8f6f4 v[154:157], v[18:25], v[198:205], v[154:157]
	v_mfma_f32_16x16x128_f8f6f4 v[146:149], v[26:33], v[198:205], v[146:149]
	v_mfma_f32_16x16x128_f8f6f4 v[138:141], v[18:25], v[214:221], v[138:141]
	v_mfma_f32_16x16x128_f8f6f4 v[130:133], v[26:33], v[214:221], v[130:133]
	v_mfma_f32_16x16x128_f8f6f4 v[122:125], v[18:25], v[222:229], v[122:125]
	v_mfma_f32_16x16x128_f8f6f4 v[114:117], v[26:33], v[222:229], v[114:117]
	v_mfma_f32_16x16x128_f8f6f4 v[106:109], v[18:25], v[230:237], v[106:109]
	v_mfma_f32_16x16x128_f8f6f4 v[98:101], v[26:33], v[230:237], v[98:101]
	s_setprio 0
	s_barrier
	v_mov_b32_e32 v162, v174
	ds_read_b128 v[198:201], v193 offset:49152
	ds_read_b128 v[202:205], v193 offset:50176
	ds_read_b128 v[214:217], v193 offset:51200
	ds_read_b128 v[218:221], v193 offset:52224
	ds_read_b128 v[222:225], v193 offset:53248
	ds_read_b128 v[226:229], v193 offset:54272
	ds_read_b128 v[230:233], v193 offset:55296
	ds_read_b128 v[234:237], v193 offset:56320
	s_mov_b32 m0, s58
	v_add_u32_e32 v162, s31, v162
	global_load_lds_dwordx4 v162, s[20:21]
	v_mov_b32_e32 v162, v174
	s_add_i32 s31, s31, s46
	v_add_u32_e32 v162, s31, v162
	s_mov_b32 m0, s59
	s_add_i32 s31, s31, s46
	global_load_lds_dwordx4 v162, s[20:21]
	v_mov_b32_e32 v162, v174
	s_mov_b32 m0, s62
	v_add_u32_e32 v162, s31, v162
	global_load_lds_dwordx4 v162, s[20:21]
	v_mov_b32_e32 v162, v174
	s_add_i32 s31, s31, s46
	v_add_u32_e32 v162, s31, v162
	s_mov_b32 m0, s63
	s_nop 0
	global_load_lds_dwordx4 v162, s[20:21]
	v_mov_b32_e32 v162, v1
	s_mov_b32 m0, s60
	v_add_u32_e32 v162, s30, v162
	global_load_lds_dwordx4 v162, s[10:11]
	v_mov_b32_e32 v162, v1
	s_add_i32 s30, s30, s45
	v_add_u32_e32 v162, s30, v162
	s_mov_b32 m0, s61
	s_nop 0
	global_load_lds_dwordx4 v162, s[10:11]
	s_waitcnt vmcnt(8)
	s_waitcnt lgkmcnt(0)
	s_barrier
	s_setprio 1
	s_waitcnt lgkmcnt(0)
	v_mfma_f32_16x16x128_f8f6f4 v[94:97], v[2:9], v[198:205], v[94:97]
	v_mfma_f32_16x16x128_f8f6f4 v[86:89], v[10:17], v[198:205], v[86:89]
	v_mfma_f32_16x16x128_f8f6f4 v[78:81], v[2:9], v[214:221], v[78:81]
	v_mfma_f32_16x16x128_f8f6f4 v[70:73], v[10:17], v[214:221], v[70:73]
	v_mfma_f32_16x16x128_f8f6f4 v[62:65], v[2:9], v[222:229], v[62:65]
	v_mfma_f32_16x16x128_f8f6f4 v[54:57], v[10:17], v[222:229], v[54:57]
	v_mfma_f32_16x16x128_f8f6f4 v[46:49], v[2:9], v[230:237], v[46:49]
	v_mfma_f32_16x16x128_f8f6f4 v[38:41], v[10:17], v[230:237], v[38:41]
	s_setprio 0
	s_setprio 1
	v_mfma_f32_16x16x128_f8f6f4 v[90:93], v[18:25], v[198:205], v[90:93]
	v_mfma_f32_16x16x128_f8f6f4 v[82:85], v[26:33], v[198:205], v[82:85]
	v_mfma_f32_16x16x128_f8f6f4 v[74:77], v[18:25], v[214:221], v[74:77]
	v_mfma_f32_16x16x128_f8f6f4 v[66:69], v[26:33], v[214:221], v[66:69]
	v_mfma_f32_16x16x128_f8f6f4 v[58:61], v[18:25], v[222:229], v[58:61]
	v_mfma_f32_16x16x128_f8f6f4 v[50:53], v[26:33], v[222:229], v[50:53]
	v_mfma_f32_16x16x128_f8f6f4 v[42:45], v[18:25], v[230:237], v[42:45]
	v_mfma_f32_16x16x128_f8f6f4 v[34:37], v[26:33], v[230:237], v[34:37]
	s_setprio 0
	s_barrier
	s_add_i32 s94, s94, 2
	s_addk_i32 s92, 0x100
	s_addk_i32 s93, 0x100
	s_cmp_ge_i32 s94, s64
	s_cbranch_scc1 .LBB0_1400

.LBB0_1839:
	s_and_b32 s90, s84, 1
	s_andn2_b64 vcc, exec, s[16:17]
	s_cbranch_vccnz .Lzs_7
	s_min_i32 s50, s89, 0x80
	s_lshr_b32 s75, s50, 5
	s_lshl_b32 s50, s86, 8
	s_ashr_i32 s51, s50, 31
	v_lshl_add_u64 v[2:3], s[50:51], 2, v[148:149]
	s_mul_i32 s50, s75, 0xf00
	s_lshl_b32 s97, s90, 10
	s_ashr_i32 s51, s50, 31
	v_lshl_add_u64 v[130:131], s[50:51], 2, v[2:3]
	s_add_i32 s97, s97, 0
	s_or_b64 s[4:5], s[6:7], s[4:5]
	s_addk_i32 s94, 0x80
	s_addk_i32 s95, 0x100
	s_mov_b32 s96, 0
	s_add_i32 s97, s97, 0x21400
	s_cmp_lg_u32 s70, s96
	s_cselect_b64 s[50:51], -1, 0
	s_or_b64 vcc, s[4:5], s[50:51]
	s_and_b64 vcc, exec, vcc
	s_cbranch_vccnz .Lphr_1
	s_mov_b32 m0, s97
	s_nop 0
	global_load_lds_dwordx4 v[130:131], off
.Lphr_1:
	ds_read_b128 v[132:135], v170
	ds_read_b128 v[136:139], v171
	ds_read_b128 v[140:143], v166
	ds_read_b128 v[154:157], v167
	ds_read_b128 v[188:191], v172
	ds_read_b128 v[192:195], v173
	ds_read_b128 v[196:199], v174
	ds_read_b128 v[200:203], v175
	s_add_i32 s75, s94, 0x80
	s_and_b64 s[50:51], s[50:51], exec
	s_cselect_b32 s50, s75, s49
	s_cselect_b32 s75, s95, s93
	s_add_i32 s51, s75, 0x80
	v_add_u32_e32 v144, s94, v183
	s_add_i32 m0, s52, 0xc000
	ds_read_b128 v[204:207], v184
	ds_read_b128 v[214:217], v184 offset:1024
	ds_read_b128 v[218:221], v184 offset:2048
	ds_read_b128 v[222:225], v184 offset:3072
	ds_read_b128 v[226:229], v184 offset:4096
	ds_read_b128 v[230:233], v184 offset:5120
	ds_read_b128 v[234:237], v184 offset:6144
	ds_read_b128 v[238:241], v184 offset:7168
	global_load_lds_dwordx4 v144, s[8:9]
	v_add_u32_e32 v144, s94, v182
	s_add_i32 m0, s52, 0xe000
	s_nop 0
	global_load_lds_dwordx4 v144, s[8:9]
	s_waitcnt vmcnt(8)
	s_waitcnt lgkmcnt(0)
	s_barrier
	s_setprio 1
	s_waitcnt lgkmcnt(0)
	v_mfma_f32_16x16x32_bf16 v[126:129], v[140:143], v[204:207], 0
	v_mfma_f32_16x16x32_bf16 v[122:125], v[136:139], v[204:207], 0
	v_mfma_f32_16x16x32_bf16 v[110:113], v[140:143], v[218:221], 0
	v_mfma_f32_16x16x32_bf16 v[106:109], v[136:139], v[218:221], 0
	v_mfma_f32_16x16x32_bf16 v[94:97], v[140:143], v[226:229], 0
	v_mfma_f32_16x16x32_bf16 v[90:93], v[136:139], v[226:229], 0
	v_mfma_f32_16x16x32_bf16 v[78:81], v[140:143], v[234:237], 0
	v_mfma_f32_16x16x32_bf16 v[74:77], v[136:139], v[234:237], 0
	v_mfma_f32_16x16x32_bf16 v[126:129], v[132:135], v[214:217], v[126:129]
	v_mfma_f32_16x16x32_bf16 v[122:125], v[188:191], v[214:217], v[122:125]
	v_mfma_f32_16x16x32_bf16 v[110:113], v[132:135], v[222:225], v[110:113]
	v_mfma_f32_16x16x32_bf16 v[106:109], v[188:191], v[222:225], v[106:109]
	v_mfma_f32_16x16x32_bf16 v[94:97], v[132:135], v[230:233], v[94:97]
	v_mfma_f32_16x16x32_bf16 v[90:93], v[188:191], v[230:233], v[90:93]
	v_mfma_f32_16x16x32_bf16 v[78:81], v[132:135], v[238:241], v[78:81]
	v_mfma_f32_16x16x32_bf16 v[74:77], v[188:191], v[238:241], v[74:77]
	s_setprio 0
	s_setprio 1
	v_mfma_f32_16x16x32_bf16 v[118:121], v[154:157], v[204:207], 0
	v_mfma_f32_16x16x32_bf16 v[114:117], v[196:199], v[204:207], 0
	v_mfma_f32_16x16x32_bf16 v[102:105], v[154:157], v[218:221], 0
	v_mfma_f32_16x16x32_bf16 v[98:101], v[196:199], v[218:221], 0
	v_mfma_f32_16x16x32_bf16 v[86:89], v[154:157], v[226:229], 0
	v_mfma_f32_16x16x32_bf16 v[82:85], v[196:199], v[226:229], 0
	v_mfma_f32_16x16x32_bf16 v[70:73], v[154:157], v[234:237], 0
	v_mfma_f32_16x16x32_bf16 v[66:69], v[196:199], v[234:237], 0
	v_mfma_f32_16x16x32_bf16 v[118:121], v[192:195], v[214:217], v[118:121]
	v_mfma_f32_16x16x32_bf16 v[114:117], v[200:203], v[214:217], v[114:117]
	v_mfma_f32_16x16x32_bf16 v[102:105], v[192:195], v[222:225], v[102:105]
	v_mfma_f32_16x16x32_bf16 v[98:101], v[200:203], v[222:225], v[98:101]
	v_mfma_f32_16x16x32_bf16 v[86:89], v[192:195], v[230:233], v[86:89]
	v_mfma_f32_16x16x32_bf16 v[82:85], v[200:203], v[230:233], v[82:85]
	v_mfma_f32_16x16x32_bf16 v[70:73], v[192:195], v[238:241], v[70:73]
	v_mfma_f32_16x16x32_bf16 v[66:69], v[200:203], v[238:241], v[66:69]
	s_setprio 0
	s_barrier
	s_mov_b32 m0, s53
	v_add_u32_e32 v144, s75, v160
	ds_read_b128 v[204:207], v184 offset:16384
	ds_read_b128 v[214:217], v184 offset:17408
	ds_read_b128 v[218:221], v184 offset:18432
	ds_read_b128 v[222:225], v184 offset:19456
	ds_read_b128 v[226:229], v184 offset:20480
	ds_read_b128 v[230:233], v184 offset:21504
	ds_read_b128 v[234:237], v184 offset:22528
	ds_read_b128 v[238:241], v184 offset:23552
	global_load_lds_dwordx4 v144, s[20:21]
	v_add_u32_e32 v144, s45, v144
	s_mov_b32 m0, s54
	s_nop 0
	global_load_lds_dwordx4 v144, s[20:21]
	v_add_u32_e32 v144, s75, v161
	s_mov_b32 m0, s55
	s_nop 0
	global_load_lds_dwordx4 v144, s[20:21]
	v_add_u32_e32 v144, s45, v144
	s_mov_b32 m0, s56
	s_nop 0
	global_load_lds_dwordx4 v144, s[20:21]
	v_add_u32_e32 v144, s50, v1
	s_mov_b32 m0, s52
	s_nop 0
	global_load_lds_dwordx4 v144, s[8:9]
	v_add_u32_e32 v144, s44, v144
	s_mov_b32 m0, s57
	s_nop 0
	global_load_lds_dwordx4 v144, s[8:9]
	s_waitcnt vmcnt(8)
	s_waitcnt lgkmcnt(0)
	s_barrier
	s_setprio 1
	s_waitcnt lgkmcnt(0)
	v_mfma_f32_16x16x32_bf16 v[62:65], v[140:143], v[204:207], 0
	v_mfma_f32_16x16x32_bf16 v[58:61], v[136:139], v[204:207], 0
	v_mfma_f32_16x16x32_bf16 v[46:49], v[140:143], v[218:221], 0
	v_mfma_f32_16x16x32_bf16 v[42:45], v[136:139], v[218:221], 0
	v_mfma_f32_16x16x32_bf16 v[30:33], v[140:143], v[226:229], 0
	v_mfma_f32_16x16x32_bf16 v[26:29], v[136:139], v[226:229], 0
	v_mfma_f32_16x16x32_bf16 v[14:17], v[140:143], v[234:237], 0
	v_mfma_f32_16x16x32_bf16 v[10:13], v[136:139], v[234:237], 0
	v_mfma_f32_16x16x32_bf16 v[62:65], v[132:135], v[214:217], v[62:65]
	v_mfma_f32_16x16x32_bf16 v[58:61], v[188:191], v[214:217], v[58:61]
	v_mfma_f32_16x16x32_bf16 v[46:49], v[132:135], v[222:225], v[46:49]
	v_mfma_f32_16x16x32_bf16 v[42:45], v[188:191], v[222:225], v[42:45]
	v_mfma_f32_16x16x32_bf16 v[30:33], v[132:135], v[230:233], v[30:33]
	v_mfma_f32_16x16x32_bf16 v[26:29], v[188:191], v[230:233], v[26:29]
	v_mfma_f32_16x16x32_bf16 v[14:17], v[132:135], v[238:241], v[14:17]
	v_mfma_f32_16x16x32_bf16 v[10:13], v[188:191], v[238:241], v[10:13]
	s_setprio 0
	s_setprio 1
	v_mfma_f32_16x16x32_bf16 v[54:57], v[154:157], v[204:207], 0
	v_mfma_f32_16x16x32_bf16 v[50:53], v[196:199], v[204:207], 0
	v_mfma_f32_16x16x32_bf16 v[38:41], v[154:157], v[218:221], 0
	v_mfma_f32_16x16x32_bf16 v[34:37], v[196:199], v[218:221], 0
	v_mfma_f32_16x16x32_bf16 v[22:25], v[154:157], v[226:229], 0
	v_mfma_f32_16x16x32_bf16 v[18:21], v[196:199], v[226:229], 0
	v_mfma_f32_16x16x32_bf16 v[6:9], v[154:157], v[234:237], 0
	v_mfma_f32_16x16x32_bf16 v[2:5], v[196:199], v[234:237], 0
	v_mfma_f32_16x16x32_bf16 v[54:57], v[192:195], v[214:217], v[54:57]
	v_mfma_f32_16x16x32_bf16 v[50:53], v[200:203], v[214:217], v[50:53]
	v_mfma_f32_16x16x32_bf16 v[38:41], v[192:195], v[222:225], v[38:41]
	v_mfma_f32_16x16x32_bf16 v[34:37], v[200:203], v[222:225], v[34:37]
	v_mfma_f32_16x16x32_bf16 v[22:25], v[192:195], v[230:233], v[22:25]
	v_mfma_f32_16x16x32_bf16 v[18:21], v[200:203], v[230:233], v[18:21]
	v_mfma_f32_16x16x32_bf16 v[6:9], v[192:195], v[238:241], v[6:9]
	v_mfma_f32_16x16x32_bf16 v[2:5], v[200:203], v[238:241], v[2:5]
	s_setprio 0
	s_barrier
	s_branch .Lmidr_1

.Lmidr_1:
	ds_read_b128 v[132:135], v176
	ds_read_b128 v[136:139], v177
	ds_read_b128 v[140:143], v168
	ds_read_b128 v[154:157], v169
	ds_read_b128 v[188:191], v178
	ds_read_b128 v[192:195], v179
	ds_read_b128 v[196:199], v180
	ds_read_b128 v[200:203], v181
	s_mov_b32 m0, s58
	v_add_u32_e32 v144, s50, v162
	ds_read_b128 v[204:207], v184 offset:32768
	ds_read_b128 v[214:217], v184 offset:33792
	ds_read_b128 v[218:221], v184 offset:34816
	ds_read_b128 v[222:225], v184 offset:35840
	ds_read_b128 v[226:229], v184 offset:36864
	ds_read_b128 v[230:233], v184 offset:37888
	ds_read_b128 v[234:237], v184 offset:38912
	ds_read_b128 v[238:241], v184 offset:39936
	global_load_lds_dwordx4 v144, s[8:9]
	v_add_u32_e32 v144, s44, v144
	s_mov_b32 m0, s59
	s_nop 0
	global_load_lds_dwordx4 v144, s[8:9]
	s_waitcnt vmcnt(8)
	s_waitcnt lgkmcnt(0)
	s_barrier
	s_setprio 1
	s_waitcnt lgkmcnt(0)
	v_mfma_f32_16x16x32_bf16 v[126:129], v[140:143], v[204:207], v[126:129]
	v_mfma_f32_16x16x32_bf16 v[122:125], v[136:139], v[204:207], v[122:125]
	v_mfma_f32_16x16x32_bf16 v[110:113], v[140:143], v[218:221], v[110:113]
	v_mfma_f32_16x16x32_bf16 v[106:109], v[136:139], v[218:221], v[106:109]
	v_mfma_f32_16x16x32_bf16 v[94:97], v[140:143], v[226:229], v[94:97]
	v_mfma_f32_16x16x32_bf16 v[90:93], v[136:139], v[226:229], v[90:93]
	v_mfma_f32_16x16x32_bf16 v[78:81], v[140:143], v[234:237], v[78:81]
	v_mfma_f32_16x16x32_bf16 v[74:77], v[136:139], v[234:237], v[74:77]
	v_mfma_f32_16x16x32_bf16 v[126:129], v[132:135], v[214:217], v[126:129]
	v_mfma_f32_16x16x32_bf16 v[122:125], v[188:191], v[214:217], v[122:125]
	v_mfma_f32_16x16x32_bf16 v[110:113], v[132:135], v[222:225], v[110:113]
	v_mfma_f32_16x16x32_bf16 v[106:109], v[188:191], v[222:225], v[106:109]
	v_mfma_f32_16x16x32_bf16 v[94:97], v[132:135], v[230:233], v[94:97]
	v_mfma_f32_16x16x32_bf16 v[90:93], v[188:191], v[230:233], v[90:93]
	v_mfma_f32_16x16x32_bf16 v[78:81], v[132:135], v[238:241], v[78:81]
	v_mfma_f32_16x16x32_bf16 v[74:77], v[188:191], v[238:241], v[74:77]
	s_setprio 0
	s_setprio 1
	v_mfma_f32_16x16x32_bf16 v[118:121], v[154:157], v[204:207], v[118:121]
	v_mfma_f32_16x16x32_bf16 v[114:117], v[196:199], v[204:207], v[114:117]
	v_mfma_f32_16x16x32_bf16 v[102:105], v[154:157], v[218:221], v[102:105]
	v_mfma_f32_16x16x32_bf16 v[98:101], v[196:199], v[218:221], v[98:101]
	v_mfma_f32_16x16x32_bf16 v[86:89], v[154:157], v[226:229], v[86:89]
	v_mfma_f32_16x16x32_bf16 v[82:85], v[196:199], v[226:229], v[82:85]
	v_mfma_f32_16x16x32_bf16 v[70:73], v[154:157], v[234:237], v[70:73]
	v_mfma_f32_16x16x32_bf16 v[66:69], v[196:199], v[234:237], v[66:69]
	v_mfma_f32_16x16x32_bf16 v[118:121], v[192:195], v[214:217], v[118:121]
	v_mfma_f32_16x16x32_bf16 v[114:117], v[200:203], v[214:217], v[114:117]
	v_mfma_f32_16x16x32_bf16 v[102:105], v[192:195], v[222:225], v[102:105]
	v_mfma_f32_16x16x32_bf16 v[98:101], v[200:203], v[222:225], v[98:101]
	v_mfma_f32_16x16x32_bf16 v[86:89], v[192:195], v[230:233], v[86:89]
	v_mfma_f32_16x16x32_bf16 v[82:85], v[200:203], v[230:233], v[82:85]
	v_mfma_f32_16x16x32_bf16 v[70:73], v[192:195], v[238:241], v[70:73]
	v_mfma_f32_16x16x32_bf16 v[66:69], v[200:203], v[238:241], v[66:69]
	s_setprio 0
	s_barrier
	s_mov_b32 m0, s64
	v_add_u32_e32 v144, s51, v160
	ds_read_b128 v[204:207], v184 offset:49152
	ds_read_b128 v[214:217], v184 offset:50176
	ds_read_b128 v[218:221], v184 offset:51200
	ds_read_b128 v[222:225], v184 offset:52224
	ds_read_b128 v[226:229], v184 offset:53248
	ds_read_b128 v[230:233], v184 offset:54272
	ds_read_b128 v[234:237], v184 offset:55296
	ds_read_b128 v[238:241], v184 offset:56320
	global_load_lds_dwordx4 v144, s[20:21]
	v_add_u32_e32 v144, s45, v144
	s_mov_b32 m0, s65
	s_nop 0
	global_load_lds_dwordx4 v144, s[20:21]
	v_add_u32_e32 v144, s51, v161
	s_mov_b32 m0, s68
	s_nop 0
	global_load_lds_dwordx4 v144, s[20:21]
	v_add_u32_e32 v144, s45, v144
	s_mov_b32 m0, s69
	s_nop 0
	global_load_lds_dwordx4 v144, s[20:21]
	v_add_u32_e32 v144, s50, v165
	s_mov_b32 m0, s66
	s_nop 0
	global_load_lds_dwordx4 v144, s[8:9]
	v_add_u32_e32 v144, s44, v144
	s_mov_b32 m0, s67
	s_nop 0
	global_load_lds_dwordx4 v144, s[8:9]
	s_waitcnt vmcnt(8)
	s_waitcnt lgkmcnt(0)
	s_barrier
	s_setprio 1
	s_waitcnt lgkmcnt(0)
	v_mfma_f32_16x16x32_bf16 v[62:65], v[140:143], v[204:207], v[62:65]
	v_mfma_f32_16x16x32_bf16 v[58:61], v[136:139], v[204:207], v[58:61]
	v_mfma_f32_16x16x32_bf16 v[46:49], v[140:143], v[218:221], v[46:49]
	v_mfma_f32_16x16x32_bf16 v[42:45], v[136:139], v[218:221], v[42:45]
	v_mfma_f32_16x16x32_bf16 v[30:33], v[140:143], v[226:229], v[30:33]
	v_mfma_f32_16x16x32_bf16 v[26:29], v[136:139], v[226:229], v[26:29]
	v_mfma_f32_16x16x32_bf16 v[14:17], v[140:143], v[234:237], v[14:17]
	v_mfma_f32_16x16x32_bf16 v[10:13], v[136:139], v[234:237], v[10:13]
	v_mfma_f32_16x16x32_bf16 v[62:65], v[132:135], v[214:217], v[62:65]
	v_mfma_f32_16x16x32_bf16 v[58:61], v[188:191], v[214:217], v[58:61]
	v_mfma_f32_16x16x32_bf16 v[46:49], v[132:135], v[222:225], v[46:49]
	v_mfma_f32_16x16x32_bf16 v[42:45], v[188:191], v[222:225], v[42:45]
	v_mfma_f32_16x16x32_bf16 v[30:33], v[132:135], v[230:233], v[30:33]
	v_mfma_f32_16x16x32_bf16 v[26:29], v[188:191], v[230:233], v[26:29]
	v_mfma_f32_16x16x32_bf16 v[14:17], v[132:135], v[238:241], v[14:17]
	v_mfma_f32_16x16x32_bf16 v[10:13], v[188:191], v[238:241], v[10:13]
	s_setprio 0
	s_setprio 1
	v_mfma_f32_16x16x32_bf16 v[54:57], v[154:157], v[204:207], v[54:57]
	v_mfma_f32_16x16x32_bf16 v[50:53], v[196:199], v[204:207], v[50:53]
	v_mfma_f32_16x16x32_bf16 v[38:41], v[154:157], v[218:221], v[38:41]
	v_mfma_f32_16x16x32_bf16 v[34:37], v[196:199], v[218:221], v[34:37]
	v_mfma_f32_16x16x32_bf16 v[22:25], v[154:157], v[226:229], v[22:25]
	v_mfma_f32_16x16x32_bf16 v[18:21], v[196:199], v[226:229], v[18:21]
	v_mfma_f32_16x16x32_bf16 v[6:9], v[154:157], v[234:237], v[6:9]
	v_mfma_f32_16x16x32_bf16 v[2:5], v[196:199], v[234:237], v[2:5]
	v_mfma_f32_16x16x32_bf16 v[54:57], v[192:195], v[214:217], v[54:57]
	v_mfma_f32_16x16x32_bf16 v[50:53], v[200:203], v[214:217], v[50:53]
	v_mfma_f32_16x16x32_bf16 v[38:41], v[192:195], v[222:225], v[38:41]
	v_mfma_f32_16x16x32_bf16 v[34:37], v[200:203], v[222:225], v[34:37]
	v_mfma_f32_16x16x32_bf16 v[22:25], v[192:195], v[230:233], v[22:25]
	v_mfma_f32_16x16x32_bf16 v[18:21], v[200:203], v[230:233], v[18:21]
	v_mfma_f32_16x16x32_bf16 v[6:9], v[192:195], v[238:241], v[6:9]
	v_mfma_f32_16x16x32_bf16 v[2:5], v[200:203], v[238:241], v[2:5]
	s_setprio 0
	s_barrier
	s_add_i32 s96, s96, 2
	s_addk_i32 s94, 0x100
	s_addk_i32 s95, 0x100
	s_cmp_ge_i32 s96, s62
	s_cbranch_scc1 .LBB0_1844

.LBB0_2935:
	s_andn2_b64 vcc, exec, s[14:15]
	s_cbranch_vccnz .Lzs_12
	s_add_i32 s28, s82, 0x80
	s_add_i32 s82, s83, 0x100
	s_mov_b32 s83, 0
	ds_read_b128 v[18:21], v180
	ds_read_b128 v[22:25], v181
	ds_read_b128 v[26:29], v188
	ds_read_b128 v[30:33], v189
	ds_read_b128 v[2:5], v182
	ds_read_b128 v[6:9], v183
	ds_read_b128 v[10:13], v190
	ds_read_b128 v[14:17], v191
	s_add_i32 s84, s28, 0x80
	s_cmp_eq_u32 s67, s83
	s_cselect_b32 s86, s25, s84
	s_cselect_b32 s87, s29, s82
	s_add_i32 s84, s86, 0x80
	s_add_i32 s85, s87, 0x80
	v_mov_b32_e32 v172, v176
	ds_read_b128 v[164:167], v196
	ds_read_b128 v[168:171], v196 offset:1024
	ds_read_b128 v[198:201], v196 offset:2048
	ds_read_b128 v[202:205], v196 offset:3072
	ds_read_b128 v[214:217], v196 offset:4096
	ds_read_b128 v[218:221], v196 offset:5120
	ds_read_b128 v[222:225], v196 offset:6144
	ds_read_b128 v[226:229], v196 offset:7168
	s_add_i32 s88, s28, s65
	v_add_u32_e32 v172, s88, v172
	s_add_i32 m0, s49, 0xc000
	s_add_i32 s88, s28, s70
	global_load_lds_dwordx4 v172, s[4:5]
	v_mov_b32_e32 v172, v176
	s_add_i32 m0, s49, 0xe000
	v_add_u32_e32 v172, s88, v172
	global_load_lds_dwordx4 v172, s[4:5]
	s_waitcnt vmcnt(8)
	s_waitcnt lgkmcnt(0)
	s_barrier
	s_setprio 1
	s_waitcnt lgkmcnt(0)
	v_mfma_f32_16x16x128_f8f6f4 v[158:161], v[18:25], v[164:171], 0
	v_mfma_f32_16x16x128_f8f6f4 v[154:157], v[26:33], v[164:171], 0
	v_mfma_f32_16x16x128_f8f6f4 v[150:153], v[18:25], v[198:205], 0
	v_mfma_f32_16x16x128_f8f6f4 v[146:149], v[26:33], v[198:205], 0
	v_mfma_f32_16x16x128_f8f6f4 v[138:141], v[18:25], v[214:221], 0
	v_mfma_f32_16x16x128_f8f6f4 v[130:133], v[26:33], v[214:221], 0
	v_mfma_f32_16x16x128_f8f6f4 v[122:125], v[18:25], v[222:229], 0
	v_mfma_f32_16x16x128_f8f6f4 v[114:117], v[26:33], v[222:229], 0
	s_setprio 0
	s_setprio 1
	v_mfma_f32_16x16x128_f8f6f4 v[142:145], v[2:9], v[164:171], 0
	v_mfma_f32_16x16x128_f8f6f4 v[134:137], v[10:17], v[164:171], 0
	v_mfma_f32_16x16x128_f8f6f4 v[126:129], v[2:9], v[198:205], 0
	v_mfma_f32_16x16x128_f8f6f4 v[118:121], v[10:17], v[198:205], 0
	v_mfma_f32_16x16x128_f8f6f4 v[110:113], v[2:9], v[214:221], 0
	v_mfma_f32_16x16x128_f8f6f4 v[106:109], v[10:17], v[214:221], 0
	v_mfma_f32_16x16x128_f8f6f4 v[102:105], v[2:9], v[222:229], 0
	v_mfma_f32_16x16x128_f8f6f4 v[98:101], v[10:17], v[222:229], 0
	s_setprio 0
	s_barrier
	v_mov_b32_e32 v172, v177
	ds_read_b128 v[164:167], v196 offset:16384
	ds_read_b128 v[168:171], v196 offset:17408
	ds_read_b128 v[198:201], v196 offset:18432
	ds_read_b128 v[202:205], v196 offset:19456
	ds_read_b128 v[214:217], v196 offset:20480
	ds_read_b128 v[218:221], v196 offset:21504
	ds_read_b128 v[222:225], v196 offset:22528
	ds_read_b128 v[226:229], v196 offset:23552
	s_mov_b32 m0, s50
	v_add_u32_e32 v172, s87, v172
	global_load_lds_dwordx4 v172, s[6:7]
	v_mov_b32_e32 v172, v177
	s_add_i32 s87, s87, s48
	v_add_u32_e32 v172, s87, v172
	s_mov_b32 m0, s51
	s_add_i32 s87, s87, s48
	global_load_lds_dwordx4 v172, s[6:7]
	v_mov_b32_e32 v172, v177
	s_mov_b32 m0, s52
	v_add_u32_e32 v172, s87, v172
	global_load_lds_dwordx4 v172, s[6:7]
	v_mov_b32_e32 v172, v177
	s_add_i32 s87, s87, s48
	v_add_u32_e32 v172, s87, v172
	s_mov_b32 m0, s53
	s_nop 0
	global_load_lds_dwordx4 v172, s[6:7]
	v_mov_b32_e32 v172, v176
	s_mov_b32 m0, s49
	v_add_u32_e32 v172, s86, v172
	global_load_lds_dwordx4 v172, s[4:5]
	v_mov_b32_e32 v172, v176
	s_add_i32 s86, s86, s47
	v_add_u32_e32 v172, s86, v172
	s_mov_b32 m0, s54
	s_nop 0
	global_load_lds_dwordx4 v172, s[4:5]
	s_waitcnt vmcnt(8)
	s_waitcnt lgkmcnt(0)
	s_barrier
	s_setprio 1
	s_waitcnt lgkmcnt(0)
	v_mfma_f32_16x16x128_f8f6f4 v[94:97], v[18:25], v[164:171], 0
	v_mfma_f32_16x16x128_f8f6f4 v[90:93], v[26:33], v[164:171], 0
	v_mfma_f32_16x16x128_f8f6f4 v[86:89], v[18:25], v[198:205], 0
	v_mfma_f32_16x16x128_f8f6f4 v[82:85], v[26:33], v[198:205], 0
	v_mfma_f32_16x16x128_f8f6f4 v[74:77], v[18:25], v[214:221], 0
	v_mfma_f32_16x16x128_f8f6f4 v[66:69], v[26:33], v[214:221], 0
	v_mfma_f32_16x16x128_f8f6f4 v[58:61], v[18:25], v[222:229], 0
	v_mfma_f32_16x16x128_f8f6f4 v[50:53], v[26:33], v[222:229], 0
	s_setprio 0
	s_setprio 1
	v_mfma_f32_16x16x128_f8f6f4 v[78:81], v[2:9], v[164:171], 0
	v_mfma_f32_16x16x128_f8f6f4 v[70:73], v[10:17], v[164:171], 0
	v_mfma_f32_16x16x128_f8f6f4 v[62:65], v[2:9], v[198:205], 0
	v_mfma_f32_16x16x128_f8f6f4 v[54:57], v[10:17], v[198:205], 0
	v_mfma_f32_16x16x128_f8f6f4 v[46:49], v[2:9], v[214:221], 0
	v_mfma_f32_16x16x128_f8f6f4 v[42:45], v[10:17], v[214:221], 0
	v_mfma_f32_16x16x128_f8f6f4 v[38:41], v[2:9], v[222:229], 0
	v_mfma_f32_16x16x128_f8f6f4 v[34:37], v[10:17], v[222:229], 0
	s_setprio 0
	s_barrier
	s_branch .Lmid_10

.Lmid_10:
	s_cmp_lg_u64 s[2:3], 0
	s_cbranch_scc0 .Ltx23_skip
	v_readfirstlane_b32 s23, v209
	s_mul_i32 s23, s23, 44
	s_add_i32 s23, s23, s79
	s_lshl_b32 s23, s23, 19
	s_mov_b32 s29, s23
